# prologue de-serialisation: conversion jobs issue their four first-tile load groups back to back (one pointer wait instead of four drains)
# baseline (speedup 1.0000x reference)
; #define TB_LOAD(R_, t_) do { const int _t = (t_); if (_t < tot) { const int _b = _t / per, _r = _t % per; ttb_load(R_, src + (size_t)_b * K_ * N_, N_, (_r % kt) * 128, (_r / kt) * 64, C.tid); } } while (0)
; __device__ __forceinline__ void ttb_load(TReg& R, const float* src, int ld, int k0, int n0, int tid) {
;     const int kr = tid >> 4, nq = tid & 15;
; #pragma unroll
;     for (int rep = 0; rep < 4; ++rep) R.v[rep] = __builtin_nontemporal_load((const f32x4*)(src + (size_t)(k0 + 4 * kr + rep) * ld + n0 + 4 * nq)); }
; template <int K_, int N_, int MAP_> __device__ __forceinline__ void tjob_b(const Ctx& C, int bid, int G, const float* src, unsigned char* dstb, int nbatch) {
;     constexpr int kt = K_ / 128, ntile = N_ / 64, per = kt * ntile; const int tot = per * nbatch;
;     TReg R0, R1, R2, R3; int kbuf = 0;
;     ...
;     TB_LOAD(R0, bid); TB_LOAD(R1, bid + G); TB_LOAD(R2, bid + 2 * G); TB_LOAD(R3, bid + 3 * G);
.LBB0_179:
	s_and_b64 s[8:9], s[2:3], exec
	v_readlane_b32 s8, v254, 2
	s_cselect_b32 s0, s8, s30
	s_add_i32 s22, s1, s0
	s_cmpk_gt_i32 s22, 0x7fff
	v_readlane_b32 s9, v254, 3
	s_cbranch_scc1 .LBB0_181
	s_ashr_i32 s8, s22, 31
	s_lshr_b32 s8, s8, 22
	s_add_i32 s9, s22, s8
	s_ashr_i32 s8, s9, 10
	s_and_b32 s9, s9, 0xfc00
	s_sub_i32 s12, s22, s9
	s_sext_i32_i16 s13, s12
	s_bfe_u32 s13, s13, 0x4001b
	s_add_i32 s13, s12, s13
	s_sext_i32_i16 s14, s13
	s_and_b32 s13, s13, 0xfff0
	s_sub_i32 s12, s12, s13
	s_ashr_i32 s9, s8, 31
	s_sext_i32_i16 s15, s12
	s_lshl_b32 s12, s14, 2
	s_lshl_b64 s[8:9], s[8:9], 25
	s_andn2_b32 s12, s12, 63
	v_and_b32_e32 v1, -4, v69
	s_ashr_i32 s13, s12, 31
	s_nop 0
	v_lshl_add_u64 v[18:19], v[66:67], 0, s[8:9]
	v_lshl_add_u32 v26, s15, 7, v1
	v_lshl_add_u64 v[18:19], s[12:13], 2, v[18:19]
	v_and_b32_e32 v20, 0xf0, v74
	v_mov_b32_e32 v21, 0
	v_ashrrev_i32_e32 v27, 31, v26
	v_lshl_add_u64 v[28:29], v[18:19], 0, v[20:21]
	v_lshlrev_b64 v[18:19], 14, v[26:27]
	v_lshl_add_u64 v[30:31], v[28:29], 0, v[18:19]
	v_or_b32_e32 v18, 1, v26
	v_ashrrev_i32_e32 v19, 31, v18
	v_lshlrev_b64 v[18:19], 14, v[18:19]
	v_lshl_add_u64 v[32:33], v[28:29], 0, v[18:19]
	global_load_dwordx4 v[18:21], v[30:31], off nt
	global_load_dwordx4 v[22:25], v[32:33], off nt
	v_or_b32_e32 v30, 2, v26
	v_ashrrev_i32_e32 v31, 31, v30
	v_or_b32_e32 v26, 3, v26
	v_lshlrev_b64 v[30:31], 14, v[30:31]
	v_ashrrev_i32_e32 v27, 31, v26
	v_lshl_add_u64 v[34:35], v[28:29], 0, v[30:31]
	v_lshlrev_b64 v[26:27], 14, v[26:27]
	v_lshl_add_u64 v[36:37], v[28:29], 0, v[26:27]
	global_load_dwordx4 v[26:29], v[34:35], off nt
	global_load_dwordx4 v[30:33], v[36:37], off nt
.LBB0_181:
	s_add_i32 s23, s22, s0
	s_cmpk_gt_i32 s23, 0x7fff
	s_cbranch_scc1 .LBB0_183
	s_ashr_i32 s8, s23, 31
	s_lshr_b32 s8, s8, 22
	s_add_i32 s9, s23, s8
	s_ashr_i32 s8, s9, 10
	s_and_b32 s9, s9, 0xfc00
	s_sub_i32 s12, s23, s9
	s_sext_i32_i16 s13, s12
	s_bfe_u32 s13, s13, 0x4001b
	s_add_i32 s13, s12, s13
	s_sext_i32_i16 s14, s13
	s_and_b32 s13, s13, 0xfff0
	s_sub_i32 s12, s12, s13
	s_ashr_i32 s9, s8, 31
	s_sext_i32_i16 s15, s12
	s_lshl_b32 s12, s14, 2
	s_lshl_b64 s[8:9], s[8:9], 25
	s_andn2_b32 s12, s12, 63
	v_and_b32_e32 v1, -4, v69
	s_ashr_i32 s13, s12, 31
	s_nop 0
	v_lshl_add_u64 v[34:35], v[66:67], 0, s[8:9]
	v_lshl_add_u32 v42, s15, 7, v1
	v_lshl_add_u64 v[34:35], s[12:13], 2, v[34:35]
	v_and_b32_e32 v36, 0xf0, v74
	v_mov_b32_e32 v37, 0
	v_ashrrev_i32_e32 v43, 31, v42
	v_lshl_add_u64 v[44:45], v[34:35], 0, v[36:37]
	v_lshlrev_b64 v[34:35], 14, v[42:43]
	v_lshl_add_u64 v[46:47], v[44:45], 0, v[34:35]
	v_or_b32_e32 v34, 1, v42
	v_ashrrev_i32_e32 v35, 31, v34
	v_lshlrev_b64 v[34:35], 14, v[34:35]
	v_lshl_add_u64 v[48:49], v[44:45], 0, v[34:35]
	global_load_dwordx4 v[34:37], v[46:47], off nt
	global_load_dwordx4 v[38:41], v[48:49], off nt
	v_or_b32_e32 v46, 2, v42
	v_ashrrev_i32_e32 v47, 31, v46
	v_or_b32_e32 v42, 3, v42
	v_lshlrev_b64 v[46:47], 14, v[46:47]
	v_ashrrev_i32_e32 v43, 31, v42
	v_lshl_add_u64 v[50:51], v[44:45], 0, v[46:47]
	v_lshlrev_b64 v[42:43], 14, v[42:43]
	v_lshl_add_u64 v[52:53], v[44:45], 0, v[42:43]
	global_load_dwordx4 v[42:45], v[50:51], off nt
	global_load_dwordx4 v[46:49], v[52:53], off nt
.LBB0_183:
	s_add_i32 s24, s23, s0
	s_cmpk_gt_i32 s24, 0x7fff
	s_cbranch_scc1 .LBB0_185
	s_ashr_i32 s8, s24, 31
	s_lshr_b32 s8, s8, 22
	s_add_i32 s9, s24, s8
	s_ashr_i32 s8, s9, 10
	s_and_b32 s9, s9, 0xfc00
	s_sub_i32 s12, s24, s9
	s_sext_i32_i16 s13, s12
	s_bfe_u32 s13, s13, 0x4001b
	s_add_i32 s13, s12, s13
	s_sext_i32_i16 s14, s13
	s_and_b32 s13, s13, 0xfff0
	s_sub_i32 s12, s12, s13
	s_ashr_i32 s9, s8, 31
	s_sext_i32_i16 s15, s12
	s_lshl_b32 s12, s14, 2
	s_lshl_b64 s[8:9], s[8:9], 25
	s_andn2_b32 s12, s12, 63
	v_and_b32_e32 v1, -4, v69
	s_ashr_i32 s13, s12, 31
	s_nop 0
	v_lshl_add_u64 v[50:51], v[66:67], 0, s[8:9]
	v_lshl_add_u32 v58, s15, 7, v1
	v_lshl_add_u64 v[50:51], s[12:13], 2, v[50:51]
	v_and_b32_e32 v52, 0xf0, v74
	v_mov_b32_e32 v53, 0
	v_ashrrev_i32_e32 v59, 31, v58
	v_lshl_add_u64 v[60:61], v[50:51], 0, v[52:53]
	v_lshlrev_b64 v[50:51], 14, v[58:59]
	v_lshl_add_u64 v[62:63], v[60:61], 0, v[50:51]
	v_or_b32_e32 v50, 1, v58
	v_ashrrev_i32_e32 v51, 31, v50
	v_lshlrev_b64 v[50:51], 14, v[50:51]
	v_lshl_add_u64 v[64:65], v[60:61], 0, v[50:51]
	global_load_dwordx4 v[50:53], v[62:63], off nt
	global_load_dwordx4 v[54:57], v[64:65], off nt
	v_or_b32_e32 v62, 2, v58
	v_ashrrev_i32_e32 v63, 31, v62
	v_or_b32_e32 v58, 3, v58
	v_lshlrev_b64 v[62:63], 14, v[62:63]
	v_ashrrev_i32_e32 v59, 31, v58
	v_lshl_add_u64 v[70:71], v[60:61], 0, v[62:63]
	v_lshlrev_b64 v[58:59], 14, v[58:59]
	v_lshl_add_u64 v[72:73], v[60:61], 0, v[58:59]
	global_load_dwordx4 v[58:61], v[70:71], off nt
	global_load_dwordx4 v[62:65], v[72:73], off nt

; #define TB_LOAD(R_, t_) do { const int _t = (t_); if (_t < tot) { const int _b = _t / per, _r = _t % per; ttb_load(R_, src + (size_t)_b * K_ * N_, N_, (_r % kt) * 128, (_r / kt) * 64, C.tid); } } while (0)
; __device__ __forceinline__ void ttb_load(TReg& R, const float* src, int ld, int k0, int n0, int tid) {
;     const int kr = tid >> 4, nq = tid & 15;
; #pragma unroll
;     for (int rep = 0; rep < 4; ++rep) R.v[rep] = __builtin_nontemporal_load((const f32x4*)(src + (size_t)(k0 + 4 * kr + rep) * ld + n0 + 4 * nq)); }
; template <int K_, int N_, int MAP_> __device__ __forceinline__ void tjob_b(const Ctx& C, int bid, int G, const float* src, unsigned char* dstb, int nbatch) {
;     constexpr int kt = K_ / 128, ntile = N_ / 64, per = kt * ntile; const int tot = per * nbatch;
;     TReg R0, R1, R2, R3; int kbuf = 0;
;     ...
;     TB_LOAD(R0, bid); TB_LOAD(R1, bid + G); TB_LOAD(R2, bid + 2 * G); TB_LOAD(R3, bid + 3 * G);
.LBB0_204:
	s_cmp_ge_i32 s22, s25
	s_cbranch_scc1 .LBB0_206
	s_ashr_i32 s8, s22, 31
	s_lshr_b32 s8, s8, 23
	s_add_i32 s9, s22, s8
	s_ashr_i32 s8, s9, 9
	s_and_b32 s9, s9, 0xfe00
	s_sub_i32 s12, s22, s9
	s_sext_i32_i16 s13, s12
	s_bfe_u32 s13, s13, 0x4001b
	s_add_i32 s13, s12, s13
	s_sext_i32_i16 s22, s13
	s_and_b32 s13, s13, 0xfff0
	s_sub_i32 s12, s12, s13
	s_ashr_i32 s9, s8, 31
	s_sext_i32_i16 s26, s12
	s_lshl_b32 s12, s22, 2
	s_lshl_b64 s[8:9], s[8:9], 24
	s_andn2_b32 s12, s12, 63
	v_and_b32_e32 v20, -4, v69
	s_ashr_i32 s13, s12, 31
	s_nop 0
	v_lshl_add_u64 v[18:19], v[66:67], 0, s[8:9]
	v_lshl_add_u32 v26, s26, 7, v20
	v_lshl_add_u64 v[18:19], s[12:13], 2, v[18:19]
	v_and_b32_e32 v20, 0xf0, v74
	v_mov_b32_e32 v21, 0
	v_ashrrev_i32_e32 v27, 31, v26
	v_lshl_add_u64 v[28:29], v[18:19], 0, v[20:21]
	v_lshlrev_b64 v[18:19], 13, v[26:27]
	v_lshl_add_u64 v[30:31], v[28:29], 0, v[18:19]
	v_or_b32_e32 v18, 1, v26
	v_ashrrev_i32_e32 v19, 31, v18
	v_lshlrev_b64 v[18:19], 13, v[18:19]
	v_lshl_add_u64 v[32:33], v[28:29], 0, v[18:19]
	global_load_dwordx4 v[18:21], v[30:31], off nt
	global_load_dwordx4 v[22:25], v[32:33], off nt
	v_or_b32_e32 v30, 2, v26
	v_ashrrev_i32_e32 v31, 31, v30
	v_or_b32_e32 v26, 3, v26
	v_lshlrev_b64 v[30:31], 13, v[30:31]
	v_ashrrev_i32_e32 v27, 31, v26
	v_lshl_add_u64 v[34:35], v[28:29], 0, v[30:31]
	v_lshlrev_b64 v[26:27], 13, v[26:27]
	v_lshl_add_u64 v[36:37], v[28:29], 0, v[26:27]
	global_load_dwordx4 v[26:29], v[34:35], off nt
	global_load_dwordx4 v[30:33], v[36:37], off nt
.LBB0_206:
	s_cmp_ge_i32 s23, s25
	s_cbranch_scc1 .LBB0_208
	s_ashr_i32 s8, s23, 31
	s_lshr_b32 s8, s8, 23
	s_add_i32 s9, s23, s8
	s_ashr_i32 s8, s9, 9
	s_and_b32 s9, s9, 0xfe00
	s_sub_i32 s12, s23, s9
	s_sext_i32_i16 s13, s12
	s_bfe_u32 s13, s13, 0x4001b
	s_add_i32 s13, s12, s13
	s_sext_i32_i16 s22, s13
	s_and_b32 s13, s13, 0xfff0
	s_sub_i32 s12, s12, s13
	s_ashr_i32 s9, s8, 31
	s_sext_i32_i16 s23, s12
	s_lshl_b32 s12, s22, 2
	s_lshl_b64 s[8:9], s[8:9], 24
	s_andn2_b32 s12, s12, 63
	v_and_b32_e32 v36, -4, v69
	s_ashr_i32 s13, s12, 31
	s_nop 0
	v_lshl_add_u64 v[34:35], v[66:67], 0, s[8:9]
	v_lshl_add_u32 v42, s23, 7, v36
	v_lshl_add_u64 v[34:35], s[12:13], 2, v[34:35]
	v_and_b32_e32 v36, 0xf0, v74
	v_mov_b32_e32 v37, 0
	v_ashrrev_i32_e32 v43, 31, v42
	v_lshl_add_u64 v[44:45], v[34:35], 0, v[36:37]
	v_lshlrev_b64 v[34:35], 13, v[42:43]
	v_lshl_add_u64 v[46:47], v[44:45], 0, v[34:35]
	v_or_b32_e32 v34, 1, v42
	v_ashrrev_i32_e32 v35, 31, v34
	v_lshlrev_b64 v[34:35], 13, v[34:35]
	v_lshl_add_u64 v[48:49], v[44:45], 0, v[34:35]
	global_load_dwordx4 v[34:37], v[46:47], off nt
	global_load_dwordx4 v[38:41], v[48:49], off nt
	v_or_b32_e32 v46, 2, v42
	v_ashrrev_i32_e32 v47, 31, v46
	v_or_b32_e32 v42, 3, v42
	v_lshlrev_b64 v[46:47], 13, v[46:47]
	v_ashrrev_i32_e32 v43, 31, v42
	v_lshl_add_u64 v[50:51], v[44:45], 0, v[46:47]
	v_lshlrev_b64 v[42:43], 13, v[42:43]
	v_lshl_add_u64 v[52:53], v[44:45], 0, v[42:43]
	global_load_dwordx4 v[42:45], v[50:51], off nt
	global_load_dwordx4 v[46:49], v[52:53], off nt
.LBB0_208:
	s_cmp_ge_i32 s24, s25
	s_cbranch_scc1 .LBB0_210
	s_ashr_i32 s8, s24, 31
	s_lshr_b32 s8, s8, 23
	s_add_i32 s9, s24, s8
	s_ashr_i32 s8, s9, 9
	s_and_b32 s9, s9, 0xfe00
	s_sub_i32 s12, s24, s9
	s_sext_i32_i16 s13, s12
	s_bfe_u32 s13, s13, 0x4001b
	s_add_i32 s13, s12, s13
	s_sext_i32_i16 s22, s13
	s_and_b32 s13, s13, 0xfff0
	s_sub_i32 s12, s12, s13
	s_ashr_i32 s9, s8, 31
	s_sext_i32_i16 s23, s12
	s_lshl_b32 s12, s22, 2
	s_lshl_b64 s[8:9], s[8:9], 24
	s_andn2_b32 s12, s12, 63
	v_and_b32_e32 v52, -4, v69
	s_ashr_i32 s13, s12, 31
	s_nop 0
	v_lshl_add_u64 v[50:51], v[66:67], 0, s[8:9]
	v_lshl_add_u32 v58, s23, 7, v52
	v_lshl_add_u64 v[50:51], s[12:13], 2, v[50:51]
	v_and_b32_e32 v52, 0xf0, v74
	v_mov_b32_e32 v53, 0
	v_ashrrev_i32_e32 v59, 31, v58
	v_lshl_add_u64 v[60:61], v[50:51], 0, v[52:53]
	v_lshlrev_b64 v[50:51], 13, v[58:59]
	v_lshl_add_u64 v[62:63], v[60:61], 0, v[50:51]
	v_or_b32_e32 v50, 1, v58
	v_ashrrev_i32_e32 v51, 31, v50
	v_lshlrev_b64 v[50:51], 13, v[50:51]
	v_lshl_add_u64 v[64:65], v[60:61], 0, v[50:51]
	global_load_dwordx4 v[50:53], v[62:63], off nt
	global_load_dwordx4 v[54:57], v[64:65], off nt
	v_or_b32_e32 v62, 2, v58
	v_ashrrev_i32_e32 v63, 31, v62
	v_or_b32_e32 v58, 3, v58
	v_lshlrev_b64 v[62:63], 13, v[62:63]
	v_ashrrev_i32_e32 v59, 31, v58
	v_lshl_add_u64 v[70:71], v[60:61], 0, v[62:63]
	v_lshlrev_b64 v[58:59], 13, v[58:59]
	v_lshl_add_u64 v[72:73], v[60:61], 0, v[58:59]
	global_load_dwordx4 v[58:61], v[70:71], off nt
	global_load_dwordx4 v[62:65], v[72:73], off nt
	s_andn2_b64 vcc, exec, s[6:7]
	s_cbranch_vccnz .LBB0_227
	s_branch .LBB0_211
